# MLA masked tile: causal mask via one per-lane distance and inline-constant compares through rotating SGPR-pair masks
# speedup vs baseline: 1.0257x; 1.0012x over previous
.LBB0_756:
	s_mul_i32 s26, s64, 0x5400
	v_add_u32_e32 v2, s26, v205
	s_waitcnt lgkmcnt(3)
	ds_read_b128 v[4:7], v2 offset:6656
	s_waitcnt lgkmcnt(1)
	ds_read_b128 v[8:11], v2
	ds_read_b128 v[12:15], v2 offset:32
	ds_read_b128 v[158:161], v2 offset:6688
	ds_read_b128 v[162:165], v2 offset:64
	ds_read_b128 v[166:169], v2 offset:6720
	ds_read_b128 v[170:173], v2 offset:96
	ds_read_b128 v[174:177], v2 offset:6752
	ds_read_b128 v[194:197], v2 offset:128
	ds_read_b128 v[210:213], v2 offset:6784
	ds_read_b128 v[214:217], v2 offset:160
	ds_read_b128 v[218:221], v2 offset:6816
	s_waitcnt lgkmcnt(10)
	v_mfma_f32_32x32x16_bf16 v[82:97], v[8:11], v[134:137], v[50:65]
	v_mfma_f32_32x32x16_bf16 v[66:81], v[4:7], v[134:137], v[50:65]
	v_add_u32_e32 v6, s26, v206
	s_waitcnt lgkmcnt(9)
	v_mfma_f32_32x32x16_bf16 v[82:97], v[12:15], v[138:141], v[82:97]
	s_waitcnt lgkmcnt(8)
	v_mfma_f32_32x32x16_bf16 v[66:81], v[158:161], v[138:141], v[66:81]
	s_waitcnt lgkmcnt(7)
	v_mfma_f32_32x32x16_bf16 v[82:97], v[162:165], v[142:145], v[82:97]
	s_waitcnt lgkmcnt(6)
	v_mfma_f32_32x32x16_bf16 v[66:81], v[166:169], v[142:145], v[66:81]
	s_waitcnt lgkmcnt(5)
	v_mfma_f32_32x32x16_bf16 v[82:97], v[170:173], v[146:149], v[82:97]
	s_waitcnt lgkmcnt(4)
	v_mfma_f32_32x32x16_bf16 v[66:81], v[174:177], v[146:149], v[66:81]
	ds_read_b64_tr_b16 v[174:175], v6 offset:13312
	ds_read_b64_tr_b16 v[176:177], v6 offset:13824
	ds_read_b64_tr_b16 v[170:171], v6 offset:14336
	ds_read_b64_tr_b16 v[172:173], v6 offset:14848
	ds_read_b64_tr_b16 v[166:167], v6 offset:15360
	ds_read_b64_tr_b16 v[168:169], v6 offset:15872
	ds_read_b64_tr_b16 v[162:163], v6 offset:16384
	ds_read_b64_tr_b16 v[164:165], v6 offset:16896
	ds_read_b64_tr_b16 v[158:159], v6 offset:17408
	ds_read_b64_tr_b16 v[160:161], v6 offset:17920
	ds_read_b64_tr_b16 v[12:13], v6 offset:18432
	ds_read_b64_tr_b16 v[14:15], v6 offset:18944
	ds_read_b64_tr_b16 v[8:9], v6 offset:19456
	ds_read_b64_tr_b16 v[10:11], v6 offset:19968
	ds_read_b64_tr_b16 v[4:5], v6 offset:20480
	ds_read_b64_tr_b16 v[6:7], v6 offset:20992
	s_waitcnt lgkmcnt(14)
	v_mfma_f32_32x32x16_bf16 v[82:97], v[194:197], v[150:153], v[82:97]
	v_mfma_f32_32x32x16_bf16 v[66:81], v[210:213], v[150:153], v[66:81]
	v_mfma_f32_32x32x16_bf16 v[82:97], v[214:217], v[154:157], v[82:97]
	v_mfma_f32_32x32x16_bf16 v[66:81], v[218:221], v[154:157], v[66:81]
	v_sub_u32_e32 v222, v208, v209
	v_add_u32_e32 v222, 59, v222
	s_cmp_lg_u32 s35, -1
	v_cmp_ge_i32_e64 vcc, v222, 32
	v_cmp_ge_i32_e64 s[28:29], v222, 1
	v_cmp_ge_i32_e64 s[30:31], v222, 0
	s_nop 5
	v_cndmask_b32_e64 v16, v243, v66, vcc
	v_cmp_ge_i32_e64 vcc, v222, 33
	v_cndmask_b32_e64 v83, v243, v83, s[28:29]
	v_cmp_ge_i32_e64 s[28:29], v222, 2
	v_cndmask_b32_e64 v82, v243, v82, s[30:31]
	v_cmp_ge_i32_e64 s[30:31], v222, 34
	v_cndmask_b32_e64 v17, v243, v67, vcc
	v_cmp_ge_i32_e64 vcc, v222, 3
	v_cndmask_b32_e64 v66, v243, v84, s[28:29]
	v_cmp_ge_i32_e64 s[28:29], v222, 35
	v_cndmask_b32_e64 v68, v243, v68, s[30:31]
	v_cmp_ge_i32_e64 s[30:31], v222, 8
	v_cndmask_b32_e64 v67, v243, v85, vcc
	v_cmp_ge_i32_e64 vcc, v222, 40
	v_cndmask_b32_e64 v69, v243, v69, s[28:29]
	v_cmp_ge_i32_e64 s[28:29], v222, 9
	v_cndmask_b32_e64 v84, v243, v86, s[30:31]
	v_cmp_ge_i32_e64 s[30:31], v222, 41
	v_cndmask_b32_e64 v70, v243, v70, vcc
	v_cmp_ge_i32_e64 vcc, v222, 10
	v_cndmask_b32_e64 v85, v243, v87, s[28:29]
	v_cmp_ge_i32_e64 s[28:29], v222, 42
	v_cndmask_b32_e64 v71, v243, v71, s[30:31]
	v_cmp_ge_i32_e64 s[30:31], v222, 11
	v_cndmask_b32_e64 v86, v243, v88, vcc
	v_cmp_ge_i32_e64 vcc, v222, 43
	v_cndmask_b32_e64 v72, v243, v72, s[28:29]
	v_cmp_ge_i32_e64 s[28:29], v222, 16
	v_cndmask_b32_e64 v87, v243, v89, s[30:31]
	v_cmp_ge_i32_e64 s[30:31], v222, 48
	v_cndmask_b32_e64 v73, v243, v73, vcc
	v_cmp_ge_i32_e64 vcc, v222, 17
	v_cndmask_b32_e64 v88, v243, v90, s[28:29]
	v_cmp_ge_i32_e64 s[28:29], v222, 49
	v_cndmask_b32_e64 v74, v243, v74, s[30:31]
	v_cmp_ge_i32_e64 s[30:31], v222, 18
	v_cndmask_b32_e64 v89, v243, v91, vcc
	v_cmp_ge_i32_e64 vcc, v222, 50
	v_cndmask_b32_e64 v75, v243, v75, s[28:29]
	v_cmp_ge_i32_e64 s[28:29], v222, 19
	v_cndmask_b32_e64 v90, v243, v92, s[30:31]
	v_cmp_ge_i32_e64 s[30:31], v222, 51
	v_cndmask_b32_e64 v76, v243, v76, vcc
	v_cmp_ge_i32_e64 vcc, v222, 24
	v_cndmask_b32_e64 v91, v243, v93, s[28:29]
	v_cmp_ge_i32_e64 s[28:29], v222, 56
	v_cndmask_b32_e64 v77, v243, v77, s[30:31]
	v_cmp_ge_i32_e64 s[30:31], v222, 25
	v_cndmask_b32_e64 v92, v243, v94, vcc
	v_cmp_ge_i32_e64 vcc, v222, 57
	v_cndmask_b32_e64 v78, v243, v78, s[28:29]
	v_cmp_ge_i32_e64 s[28:29], v222, 26
	v_cndmask_b32_e64 v93, v243, v95, s[30:31]
	v_cmp_ge_i32_e64 s[30:31], v222, 58
	v_cndmask_b32_e64 v79, v243, v79, vcc
	v_cmp_ge_i32_e64 vcc, v222, 27
	v_cndmask_b32_e64 v94, v243, v96, s[28:29]
	v_cmp_ge_i32_e64 s[28:29], v222, 59
	v_cndmask_b32_e64 v80, v243, v80, s[30:31]
	v_cndmask_b32_e64 v95, v243, v97, vcc
	v_cndmask_b32_e64 v81, v243, v81, s[28:29]
	v_max3_f32 v96, v16, v17, v68
	v_max3_f32 v2, v82, v83, v66
	v_max3_f32 v2, v2, v67, v84
	v_max3_f32 v96, v96, v69, v70
	v_max3_f32 v2, v2, v85, v86
	v_max3_f32 v96, v96, v71, v72
	v_max3_f32 v2, v2, v87, v88
	v_max3_f32 v96, v96, v73, v74
	v_max3_f32 v2, v2, v89, v90
	v_max3_f32 v96, v96, v75, v76
	v_max3_f32 v2, v2, v91, v92
	v_max3_f32 v96, v96, v77, v78
	v_max3_f32 v2, v2, v93, v94
	v_max3_f32 v96, v96, v79, v80
	v_max_f32_e32 v97, v95, v81
	v_max3_f32 v2, v2, v96, v97
	ds_bpermute_b32 v96, v223, v2
	s_waitcnt lgkmcnt(0)
	v_max_f32_e32 v96, v2, v96
	s_cbranch_scc0 .Lmla_m_first
	v_cmp_lt_f32_e32 vcc, s81, v96
	s_cbranch_vccz .LBB0_744
	v_max_f32_e32 v2, v96, v96
	v_max_f32_e32 v2, 0, v2
	s_branch .Lmla_m_resc
